# baseline (speedup 1.0000x reference)
.LBB3_6:
	v_lshlrev_b32_e32 v1, 4, v0
	v_and_b32_e32 v2, 32, v0
	v_bitop3_b32 v1, v1, v2, 48 bitop3:0x6c
	v_bfe_u32 v3, v0, 2, 4
	v_and_or_b32 v2, v0, 64, v1
	v_lshrrev_b32_e32 v1, 3, v0
	s_lshl_b32 s38, s6, 3
	s_lshl_b32 s23, s4, 1
	v_and_or_b32 v4, v1, 48, v3
	s_abs_i32 s39, s38
	v_mad_u64_u32 v[128:129], s[12:13], s23, v4, v[2:3]
	v_cvt_f32_u32_e32 v4, s39
	s_sub_i32 s25, 0, s39
	s_add_i32 s22, s7, s22
	s_ashr_i32 s7, s22, 31
	v_rcp_iflag_f32_e32 v4, v4
	s_bfe_i32 s40, s6, 0x1001c
	s_xor_b32 s6, s7, s40
	s_abs_i32 s7, s22
	v_mul_f32_e32 v4, 0x4f7ffffe, v4
	v_cvt_u32_f32_e32 v4, v4
	s_ashr_i32 s21, s16, 31
	s_lshr_b32 s19, s3, 6
	s_ashr_i32 s17, s4, 31
	v_readfirstlane_b32 s41, v4
	s_mul_i32 s25, s25, s41
	s_mul_hi_u32 s25, s41, s25
	s_add_i32 s41, s41, s25
	s_mul_hi_u32 s25, s7, s41
	s_mul_i32 s28, s25, s39
	s_mov_b32 s16, s4
	s_sub_i32 s7, s7, s28
	s_ashr_i32 s26, s33, 31
	s_lshr_b32 s18, s3, 8
	s_lshl_b64 s[12:13], s[16:17], 8
	s_lshl_b32 s27, s19, 10
	s_add_i32 s28, s25, 1
	s_sub_i32 s29, s7, s39
	s_cmp_ge_u32 s7, s39
	s_cselect_b32 s25, s28, s25
	s_cselect_b32 s7, s29, s7
	s_add_i32 s28, s25, 1
	s_cmp_ge_u32 s7, s39
	s_cselect_b32 s7, s28, s25
	s_xor_b32 s7, s7, s6
	s_sub_i32 s25, s7, s6
	s_lshl_b32 s28, s25, 3
	s_sub_i32 s6, s5, s28
	s_min_i32 s29, s6, 8
	s_abs_i32 s30, s29
	v_cvt_f32_u32_e32 v4, s30
	v_or_b32_e32 v1, 64, v1
	s_movk_i32 s24, 0x70
	v_and_or_b32 v1, v1, s24, v3
	v_mad_u64_u32 v[130:131], s[6:7], s23, v1, v[2:3]
	v_rcp_iflag_f32_e32 v1, v4
	s_sub_i32 s23, 0, s30
	s_mul_i32 s25, s25, s38
	s_sub_i32 s6, s22, s25
	v_mul_f32_e32 v1, 0x4f7ffffe, v1
	v_cvt_u32_f32_e32 v1, v1
	s_abs_i32 s22, s6
	s_xor_b32 s7, s6, s29
	s_ashr_i32 s7, s7, 31
	v_readfirstlane_b32 s24, v1
	s_mul_i32 s23, s23, s24
	s_mul_hi_u32 s23, s24, s23
	s_add_i32 s24, s24, s23
	s_mul_hi_u32 s23, s22, s24
	s_mul_i32 s24, s23, s30
	s_sub_i32 s22, s22, s24
	s_add_i32 s24, s23, 1
	s_sub_i32 s25, s22, s30
	s_cmp_ge_u32 s22, s30
	s_cselect_b32 s23, s24, s23
	s_cselect_b32 s22, s25, s22
	s_add_i32 s24, s23, 1
	s_cmp_ge_u32 s22, s30
	s_cselect_b32 s22, s24, s23
	s_xor_b32 s22, s22, s7
	s_sub_i32 s46, s22, s7
	s_mul_i32 s7, s46, s29
	s_sub_i32 s6, s6, s7
	s_add_i32 s45, s6, s28
	s_ashr_i32 s6, s45, 31
	s_mul_i32 s6, s12, s6
	s_mul_hi_u32 s7, s12, s45
	s_add_i32 s22, s7, s6
	s_lshr_b64 s[6:7], s[16:17], 24
	s_mul_i32 s6, s6, s45
	s_add_i32 s6, s22, s6
	s_mul_i32 s7, s12, s45
	s_waitcnt lgkmcnt(0)
	s_add_u32 s22, s8, s7
	s_addc_u32 s23, s9, s6
	s_ashr_i32 s24, s46, 31
	s_lshl_b64 s[6:7], s[16:17], 9
	s_mul_i32 s24, s6, s24
	s_mul_hi_u32 s25, s6, s46
	s_add_i32 s28, s25, s24
	s_lshr_b64 s[24:25], s[16:17], 23
	s_add_i32 s42, s27, 0
	s_mul_i32 s16, s24, s46
	s_mov_b32 m0, s42
	s_add_i32 s28, s28, s16
	s_mul_i32 s16, s6, s46
	global_load_lds_dwordx4 v128, s[22:23]
	s_add_i32 m0, s42, 0x2000
	s_add_u32 s24, s10, s16
	global_load_lds_dwordx4 v130, s[22:23]
	s_addc_u32 s25, s11, s28
	s_add_i32 m0, s42, 0x4000
	v_mov_b32_e32 v129, 0
	global_load_lds_dwordx4 v128, s[24:25]
	s_add_i32 m0, s42, 0x6000
	s_add_u32 s28, s24, s12
	global_load_lds_dwordx4 v130, s[24:25]
	s_addc_u32 s29, s25, s13
	s_add_i32 m0, s42, 0x8000
	v_mov_b32_e32 v131, v129
	global_load_lds_dwordx4 v128, s[28:29]
	s_add_i32 m0, s42, 0xa000
	v_lshl_add_u64 v[2:3], s[22:23], 0, v[128:129]
	v_lshl_add_u64 v[10:11], s[28:29], 0, v[128:129]
	v_lshl_add_u64 v[12:13], s[28:29], 0, v[130:131]
	global_load_lds_dwordx4 v130, s[28:29]
	s_mov_b64 s[28:29], 0x80
	v_lshl_add_u64 v[4:5], s[22:23], 0, v[130:131]
	s_add_i32 m0, s42, 0xc000
	v_lshl_add_u64 v[2:3], v[2:3], 0, s[28:29]
	v_lshl_add_u64 v[6:7], s[24:25], 0, v[128:129]
	global_load_lds_dwordx4 v[2:3], off
	v_lshl_add_u64 v[2:3], v[4:5], 0, s[28:29]
	s_add_i32 m0, s42, 0xe000
	v_lshl_add_u64 v[8:9], s[24:25], 0, v[130:131]
	global_load_lds_dwordx4 v[2:3], off
	s_add_i32 m0, s42, 0x10000
	v_lshl_add_u64 v[2:3], v[6:7], 0, s[28:29]
	global_load_lds_dwordx4 v[2:3], off
	v_lshl_add_u64 v[2:3], v[8:9], 0, s[28:29]
	s_add_i32 m0, s42, 0x12000
	s_nop 0
	global_load_lds_dwordx4 v[2:3], off
	s_add_i32 m0, s42, 0x14000
	v_lshl_add_u64 v[2:3], v[10:11], 0, s[28:29]
	global_load_lds_dwordx4 v[2:3], off
	v_lshl_add_u64 v[2:3], v[12:13], 0, s[28:29]
	s_add_i32 m0, s42, 0x16000
	global_load_lds_dwordx4 v[2:3], off
	s_mov_b64 s[28:29], 0x100
	v_lshl_add_u64 v[2:3], s[22:23], 0, v[128:129]
	s_add_i32 m0, s42, 0x18000
	v_lshl_add_u64 v[2:3], v[2:3], 0, s[28:29]
	global_load_lds_dwordx4 v[2:3], off
	v_lshl_add_u64 v[2:3], v[4:5], 0, s[28:29]
	s_add_i32 m0, s42, 0x1a000
	s_nop 0
	global_load_lds_dwordx4 v[2:3], off
	s_add_i32 m0, s42, 0x1c000
	v_lshl_add_u64 v[2:3], v[6:7], 0, s[28:29]
	global_load_lds_dwordx4 v[2:3], off
	v_lshl_add_u64 v[2:3], v[8:9], 0, s[28:29]
	s_add_i32 m0, s42, 0x1e000
	s_nop 0
	global_load_lds_dwordx4 v[2:3], off
	s_add_i32 m0, s42, 0x20000
	v_lshl_add_u64 v[2:3], v[10:11], 0, s[28:29]
	global_load_lds_dwordx4 v[2:3], off
	v_lshl_add_u64 v[2:3], v[12:13], 0, s[28:29]
	s_add_i32 m0, s42, 0x22000
	s_mov_b32 s56, 1
	global_load_lds_dwordx4 v[2:3], off
	s_cmp_lg_u32 s18, 1
	s_cbranch_scc1 .LBB3_8
	s_barrier
.LBB3_8:
	s_xor_b32 s16, s21, s26
	s_mul_i32 s21, s20, s14
	s_sub_i32 s15, s15, s21
	s_add_i32 s21, s20, 1
	s_sub_i32 s26, s15, s14
	s_cmp_ge_u32 s15, s14
	s_cselect_b32 s20, s21, s20
	s_cselect_b32 s15, s26, s15
	s_add_i32 s21, s20, 1
	s_cmp_ge_u32 s15, s14
	s_cselect_b32 s14, s21, s20
	s_xor_b32 s14, s14, s16
	s_waitcnt vmcnt(12)
	s_sub_i32 s43, s14, s16
	s_cmp_lt_i32 s43, 1
	s_barrier
	s_barrier
	s_cbranch_scc1 .LBB3_27
	s_load_dwordx2 s[14:15], s[0:1], 0x20
	s_load_dword s44, s[0:1], 0x28
	v_bfe_u32 v1, v0, 4, 2
	s_lshl_b32 s1, s19, 5
	v_and_b32_e32 v2, 15, v0
	v_lshlrev_b32_e32 v3, 4, v1
	s_and_b32 s1, s1, 0x60
	v_lshlrev_b32_e32 v4, 6, v0
	s_movk_i32 s16, 0x3c0
	v_lshlrev_b32_e32 v0, 2, v0
	v_lshl_or_b32 v132, s18, 6, v2
	v_lshl_or_b32 v2, v2, 6, v3
	v_and_or_b32 v3, v4, s16, v3
	s_lshl_b32 s16, s1, 7
	v_and_b32_e32 v0, 32, v0
	v_bitop3_b32 v3, s16, v3, v0 bitop3:0xf6
	s_lshr_b32 s16, s17, 26
	s_lshl_b32 s0, s18, 13
	s_add_i32 s16, s4, s16
	s_ashr_i32 s47, s16, 6
	s_add_i32 s0, s0, 0
	s_cmp_gt_i32 s4, 63
	v_xad_u32 v133, v2, v0, s0
	v_lshl_or_b32 v134, v1, 2, s1
	s_cselect_b64 s[0:1], -1, 0
	v_cndmask_b32_e64 v0, 0, 1, s[0:1]
	s_mov_b32 s17, 0
	v_add_u32_e32 v135, 0, v3
	s_mov_b32 s51, 0x18000
	v_cmp_ne_u32_e64 s[0:1], 1, v0
	s_mov_b32 s4, 0
	s_mov_b32 s48, 0
	s_mov_b64 s[18:19], s[22:23]
	s_branch .LBB3_12

.LBB3_25:
	s_andn2_b64 vcc, exec, s[30:31]
	s_cbranch_vccnz .LBB3_22
	s_cmp_eq_u32 s56, 0
	s_cbranch_scc1 .Lhg_stage
	s_mov_b32 s56, 0
	s_branch .Lhg_nostage
.Lhg_stage:
	s_and_b64 s[30:31], s[28:29], exec
	s_cselect_b32 s16, 0, s47
	s_cselect_b32 s53, s25, s21
	s_cselect_b32 s54, s24, s20
	s_sub_i32 s16, s52, s16
	s_add_i32 s16, s16, 2
	s_lshl_b64 s[30:31], s[16:17], 7
	s_add_u32 s54, s54, s30
	s_addc_u32 s55, s53, s31
	s_and_b64 s[28:29], s[28:29], exec
	s_cselect_b32 s28, s22, s18
	s_cselect_b32 s16, s23, s19
	s_add_u32 s28, s28, s30
	s_addc_u32 s29, s16, s31
	s_add_i32 s16, s42, s51
	v_lshl_add_u64 v[136:137], s[28:29], 0, v[128:129]
	s_mov_b32 m0, s16
	s_nop 0
	global_load_lds_dwordx4 v[136:137], off
	v_lshl_add_u64 v[136:137], s[28:29], 0, v[130:131]
	s_add_i32 m0, s16, 0x2000
	s_nop 0
	global_load_lds_dwordx4 v[136:137], off
	s_add_i32 m0, s16, 0x4000
	v_lshl_add_u64 v[136:137], s[54:55], 0, v[128:129]
	global_load_lds_dwordx4 v[136:137], off
	s_add_i32 m0, s16, 0x6000
	s_add_u32 s28, s54, s12
	v_lshl_add_u64 v[136:137], s[54:55], 0, v[130:131]
	s_addc_u32 s29, s55, s13
	global_load_lds_dwordx4 v[136:137], off
	s_add_i32 m0, s16, 0x8000
	v_lshl_add_u64 v[136:137], s[28:29], 0, v[128:129]
	global_load_lds_dwordx4 v[136:137], off
	v_lshl_add_u64 v[136:137], s[28:29], 0, v[130:131]
	s_add_i32 m0, s16, 0xa000
	s_nop 0
	global_load_lds_dwordx4 v[136:137], off
.Lhg_nostage:
	s_waitcnt vmcnt(6)
	s_branch .LBB3_22

	.amdhsa_kernel _Z12hgemm_kernelIN2hg6EpiF32EEvNS0_4GemmET_
		.amdhsa_group_segment_fixed_size 0
		.amdhsa_private_segment_fixed_size 0
		.amdhsa_kernarg_size 304
		.amdhsa_user_sgpr_count 2
		.amdhsa_user_sgpr_dispatch_ptr 0
		.amdhsa_user_sgpr_queue_ptr 0
		.amdhsa_user_sgpr_kernarg_segment_ptr 1
		.amdhsa_user_sgpr_dispatch_id 0
		.amdhsa_user_sgpr_kernarg_preload_length 0
		.amdhsa_user_sgpr_kernarg_preload_offset 0
		.amdhsa_user_sgpr_private_segment_size 0
		.amdhsa_uses_dynamic_stack 0
		.amdhsa_enable_private_segment 0
		.amdhsa_system_sgpr_workgroup_id_x 1
		.amdhsa_system_sgpr_workgroup_id_y 0
		.amdhsa_system_sgpr_workgroup_id_z 0
		.amdhsa_system_sgpr_workgroup_info 0
		.amdhsa_system_vgpr_workitem_id 0
		.amdhsa_next_free_vgpr 138
		.amdhsa_next_free_sgpr 57
		.amdhsa_accum_offset 140
		.amdhsa_reserve_vcc 1
		.amdhsa_float_round_mode_32 0
		.amdhsa_float_round_mode_16_64 0
		.amdhsa_float_denorm_mode_32 3
		.amdhsa_float_denorm_mode_16_64 3
		.amdhsa_dx10_clamp 1
		.amdhsa_ieee_mode 1
		.amdhsa_fp16_overflow 0
		.amdhsa_tg_split 0
		.amdhsa_exception_fp_ieee_invalid_op 0
		.amdhsa_exception_fp_denorm_src 0
		.amdhsa_exception_fp_ieee_div_zero 0
		.amdhsa_exception_fp_ieee_overflow 0
		.amdhsa_exception_fp_ieee_underflow 0
		.amdhsa_exception_fp_ieee_inexact 0
		.amdhsa_exception_int_div_zero 0
	.end_amdhsa_kernel

amdhsa.kernels:
  - .agpr_count:     0
    .args:
      - .actual_access:  read_only
        .address_space:  global
        .offset:         0
        .size:           8
        .value_kind:     global_buffer
      - .actual_access:  read_only
        .address_space:  global
        .offset:         8
        .size:           8
        .value_kind:     global_buffer
      - .actual_access:  read_only
        .address_space:  global
        .offset:         16
        .size:           8
        .value_kind:     global_buffer
      - .actual_access:  read_only
        .address_space:  global
        .offset:         24
        .size:           8
        .value_kind:     global_buffer
      - .actual_access:  read_only
        .address_space:  global
        .offset:         32
        .size:           8
        .value_kind:     global_buffer
      - .actual_access:  read_only
        .address_space:  global
        .offset:         40
        .size:           8
        .value_kind:     global_buffer
      - .address_space:  global
        .offset:         48
        .size:           8
        .value_kind:     global_buffer
      - .address_space:  global
        .offset:         56
        .size:           8
        .value_kind:     global_buffer
      - .address_space:  global
        .offset:         64
        .size:           8
        .value_kind:     global_buffer
      - .address_space:  global
        .offset:         72
        .size:           8
        .value_kind:     global_buffer
    .group_segment_fixed_size: 0
    .kernarg_segment_align: 8
    .kernarg_segment_size: 80
    .language:       OpenCL C
    .language_version:
      - 2
      - 0
    .max_flat_workgroup_size: 256
    .name:           _Z11prep_kernelPKfPKiS0_S0_S0_S0_PtS3_S3_P15HIP_vector_typeIfLj2EE
    .private_segment_fixed_size: 0
    .sgpr_count:     44
    .sgpr_spill_count: 0
    .symbol:         _Z11prep_kernelPKfPKiS0_S0_S0_S0_PtS3_S3_P15HIP_vector_typeIfLj2EE.kd
    .uniform_work_group_size: 1
    .uses_dynamic_stack: false
    .vgpr_count:     40
    .vgpr_spill_count: 0
    .wavefront_size: 64
  - .agpr_count:     0
    .args:
      - .offset:         0
        .size:           32
        .value_kind:     by_value
      - .offset:         32
        .size:           24
        .value_kind:     by_value
      - .offset:         56
        .size:           32
        .value_kind:     by_value
      - .offset:         88
        .size:           24
        .value_kind:     by_value
      - .offset:         112
        .size:           4
        .value_kind:     hidden_block_count_x
      - .offset:         116
        .size:           4
        .value_kind:     hidden_block_count_y
      - .offset:         120
        .size:           4
        .value_kind:     hidden_block_count_z
      - .offset:         124
        .size:           2
        .value_kind:     hidden_group_size_x
      - .offset:         126
        .size:           2
        .value_kind:     hidden_group_size_y
      - .offset:         128
        .size:           2
        .value_kind:     hidden_group_size_z
      - .offset:         130
        .size:           2
        .value_kind:     hidden_remainder_x
      - .offset:         132
        .size:           2
        .value_kind:     hidden_remainder_y
      - .offset:         134
        .size:           2
        .value_kind:     hidden_remainder_z
      - .offset:         152
        .size:           8
        .value_kind:     hidden_global_offset_x
      - .offset:         160
        .size:           8
        .value_kind:     hidden_global_offset_y
      - .offset:         168
        .size:           8
        .value_kind:     hidden_global_offset_z
      - .offset:         176
        .size:           2
        .value_kind:     hidden_grid_dims
      - .offset:         232
        .size:           4
        .value_kind:     hidden_dynamic_lds_size
    .group_segment_fixed_size: 0
    .kernarg_segment_align: 8
    .kernarg_segment_size: 368
    .language:       OpenCL C
    .language_version:
      - 2
      - 0
    .max_flat_workgroup_size: 512
    .name:           _Z10qkv_kernelN3pg84GemmENS_7EpiRopeEN2hg4GemmENS2_7EpiRopeE
    .private_segment_fixed_size: 0
    .sgpr_count:     99
    .sgpr_spill_count: 0
    .symbol:         _Z10qkv_kernelN3pg84GemmENS_7EpiRopeEN2hg4GemmENS2_7EpiRopeE.kd
    .uniform_work_group_size: 1
    .uses_dynamic_stack: false
    .vgpr_count:     240
    .vgpr_spill_count: 0
    .wavefront_size: 64
  - .agpr_count:     0
    .args:
      - .address_space:  global
        .offset:         0
        .size:           8
        .value_kind:     global_buffer
      - .address_space:  global
        .offset:         8
        .size:           8
        .value_kind:     global_buffer
      - .address_space:  global
        .offset:         16
        .size:           8
        .value_kind:     global_buffer
      - .address_space:  global
        .offset:         24
        .size:           8
        .value_kind:     global_buffer
    .group_segment_fixed_size: 0
    .kernarg_segment_align: 8
    .kernarg_segment_size: 32
    .language:       OpenCL C
    .language_version:
      - 2
      - 0
    .max_flat_workgroup_size: 512
    .name:           _Z11attn_kernelPKDF16_S0_S0_PDF16_
    .private_segment_fixed_size: 0
    .sgpr_count:     62
    .sgpr_spill_count: 0
    .symbol:         _Z11attn_kernelPKDF16_S0_S0_PDF16_.kd
    .uniform_work_group_size: 1
    .uses_dynamic_stack: false
    .vgpr_count:     243
    .vgpr_spill_count: 0
    .wavefront_size: 64
  - .agpr_count:     0
    .args:
      - .offset:         0
        .size:           32
        .value_kind:     by_value
      - .offset:         32
        .size:           16
        .value_kind:     by_value
      - .offset:         48
        .size:           4
        .value_kind:     hidden_block_count_x
      - .offset:         52
        .size:           4
        .value_kind:     hidden_block_count_y
      - .offset:         56
        .size:           4
        .value_kind:     hidden_block_count_z
      - .offset:         60
        .size:           2
        .value_kind:     hidden_group_size_x
      - .offset:         62
        .size:           2
        .value_kind:     hidden_group_size_y
      - .offset:         64
        .size:           2
        .value_kind:     hidden_group_size_z
      - .offset:         66
        .size:           2
        .value_kind:     hidden_remainder_x
      - .offset:         68
        .size:           2
        .value_kind:     hidden_remainder_y
      - .offset:         70
        .size:           2
        .value_kind:     hidden_remainder_z
      - .offset:         88
        .size:           8
        .value_kind:     hidden_global_offset_x
      - .offset:         96
        .size:           8
        .value_kind:     hidden_global_offset_y
      - .offset:         104
        .size:           8
        .value_kind:     hidden_global_offset_z
      - .offset:         112
        .size:           2
        .value_kind:     hidden_grid_dims
      - .offset:         168
        .size:           4
        .value_kind:     hidden_dynamic_lds_size
    .group_segment_fixed_size: 0
    .kernarg_segment_align: 8
    .kernarg_segment_size: 304
    .language:       OpenCL C
    .language_version:
      - 2
      - 0
    .max_flat_workgroup_size: 512
    .name:           _Z12hgemm_kernelIN2hg6EpiF32EEvNS0_4GemmET_
    .private_segment_fixed_size: 0
    .sgpr_count:     63
    .sgpr_spill_count: 0
    .symbol:         _Z12hgemm_kernelIN2hg6EpiF32EEvNS0_4GemmET_.kd
    .uniform_work_group_size: 1
    .uses_dynamic_stack: false
    .vgpr_count:     138
    .vgpr_spill_count: 0
    .wavefront_size: 64
